# attention item prologue: both query sub-tile loads issued together (one memory round trip instead of two), on top of permlane max + LRU rebalance
# baseline (speedup 1.0000x reference)
; __device__ __forceinline__ float lo16(unsigned u) { return __uint_as_float(u << 16); }
; __device__ __forceinline__ float hi16(unsigned u) { return __uint_as_float(u & 0xffff0000u); }
; __device__ void phase_swa_mfma(const Params& p, int l, char* smem, int vb, int nvb, int pend, int oz) {
;     ...
;         for (int qt2 = 0; qt2 < 2; ++qt2) {
;             const int tq = qt * 64 + 32 * qsub + 16 * qt2 + li;
;             const bf16_t* qp = U + (qbase + tq) * LDU + C_SQ + hq * 64 + 8 * g;
;             const u32x4 r0 = *(const u32x4*)qp, r1 = *(const u32x4*)(qp + 32);
;             float x1[8], x2[8];
; #pragma unroll
;             for (int w = 0; w < 4; ++w) {
;                 x1[2 * w] = lo16(r0[w]); x1[2 * w + 1] = hi16(r0[w]);
;                 x2[2 * w] = lo16(r1[w]); x2[2 * w + 1] = hi16(r1[w]);
;             }
;             if (!cq) {
;                 const float pos = (g < 2) ? (float)(tq >> 6) : (float)(tq & 63);
; #pragma unroll
;                 for (int j = 0; j < 8; ++j) {
;                     float rev = pos * invq[j];
;                     rev -= floorf(rev);
;                     const float cs = __builtin_amdgcn_cosf(rev), sn = __builtin_amdgcn_sinf(rev);
;                     const float a1 = x1[j], a2 = x2[j];
;                     x1[j] = a1 * cs - a2 * sn;
;                     x2[j] = a1 * sn + a2 * cs;
;                 }
;             }
.LBB0_183:
	s_and_b32 s2, s21, 1
	s_lshl_b32 s80, s2, 1
	s_ashr_i32 s21, s20, 31
	s_add_i32 s80, s80, s55
	s_lshl_b64 s[50:51], s[20:21], 8
	s_add_u32 s44, s50, 0x4000
	s_addc_u32 s45, s51, 0
	s_lshl_b64 s[46:47], s[20:21], 11
	s_and_b64 s[20:21], s[40:41], exec
	s_cselect_b32 s21, s47, s45
	s_cselect_b32 s20, s46, s44
	v_or_b32_e32 v120, s24, v166
	v_mov_b32_e32 v121, v3
	v_lshl_add_u64 v[6:7], s[20:21], 0, v[120:121]
	v_mov_b64_e32 v[4:5], s[34:35]
	v_mad_u64_u32 v[4:5], s[24:25], v6, s92, v[4:5]
	v_mad_i32_i24 v5, v7, s92, v5
	s_lshl_b32 s96, s80, 7
	v_lshl_add_u64 v[8:9], v[4:5], 0, s[96:97]
	v_lshlrev_b32_e32 v6, 1, v100
	v_mov_b32_e32 v7, v3
	v_lshl_add_u64 v[12:13], v[8:9], 0, v[6:7]
	v_add_co_u32_e32 v8, vcc, s22, v12
	s_mov_b64 s[4:5], 0x1400
	s_nop 0
	v_addc_co_u32_e32 v9, vcc, 0, v13, vcc
	v_lshl_add_u64 v[12:13], v[12:13], 0, s[4:5]
	s_mov_b64 s[4:5], 0x1a800
	v_lshl_add_u64 v[238:239], v[8:9], 0, s[4:5]
	v_lshl_add_u64 v[240:241], v[12:13], 0, s[4:5]
	s_mov_b64 s[4:5], 0x1400
	global_load_dwordx4 v[8:11], v[8:9], off offset:1024
	v_cndmask_b32_e64 v7, 0, 1, s[40:41]
	global_load_dwordx4 v[12:15], v[12:13], off offset:64
	global_load_dwordx4 v[226:229], v[238:239], off offset:1024
	global_load_dwordx4 v[230:233], v[240:241], off offset:64
	v_cmp_ne_u32_e64 s[42:43], 1, v7
	s_andn2_b64 vcc, exec, s[40:41]
	s_waitcnt vmcnt(2)
	v_and_b32_e32 v28, 0xffff0000, v8
	v_lshlrev_b32_e32 v29, 16, v8
	v_and_b32_e32 v32, 0xffff0000, v12
	v_lshlrev_b32_e32 v33, 16, v12
	v_and_b32_e32 v42, 0xffff0000, v9
	v_lshlrev_b32_e32 v43, 16, v9
	v_and_b32_e32 v30, 0xffff0000, v13
	v_lshlrev_b32_e32 v31, 16, v13
	v_and_b32_e32 v40, 0xffff0000, v10
	v_lshlrev_b32_e32 v41, 16, v10
	v_and_b32_e32 v34, 0xffff0000, v14
	v_lshlrev_b32_e32 v35, 16, v14
	v_and_b32_e32 v38, 0xffff0000, v11
	v_lshlrev_b32_e32 v39, 16, v11
	v_and_b32_e32 v36, 0xffff0000, v15
	v_lshlrev_b32_e32 v37, 16, v15
	s_cbranch_vccnz .LBB0_185
	v_and_b32_e32 v7, 47, v120
	v_mov_b32_e32 v8, s57
	v_cndmask_b32_e64 v7, v7, v8, s[36:37]
	v_cvt_f32_u32_e32 v7, v7
	v_mul_f32_e32 v8, v1, v7
	v_floor_f32_e32 v8, v8
	v_fma_f32 v8, v1, v7, -v8
	v_cos_f32_e32 v9, v8
	v_sin_f32_e32 v11, v8
	v_mul_f32_e32 v8, v103, v7
	v_floor_f32_e32 v8, v8
	v_fma_f32 v10, v103, v7, -v8
	v_cos_f32_e32 v8, v10
	v_sin_f32_e32 v10, v10
	s_nop 0
	v_pk_mul_f32 v[12:13], v[10:11], v[32:33]
	s_nop 0
	v_pk_fma_f32 v[12:13], v[8:9], v[28:29], v[12:13] neg_lo:[0,0,1] neg_hi:[0,0,1]
	v_pk_mul_f32 v[8:9], v[8:9], v[32:33]
	s_nop 0
	v_pk_fma_f32 v[32:33], v[10:11], v[28:29], v[8:9]
	v_mul_f32_e32 v8, v148, v7
	v_floor_f32_e32 v8, v8
	v_fma_f32 v8, v148, v7, -v8
	v_cos_f32_e32 v9, v8
	v_sin_f32_e32 v11, v8
	v_mul_f32_e32 v8, v150, v7
	v_floor_f32_e32 v8, v8
	v_fma_f32 v10, v150, v7, -v8
	v_cos_f32_e32 v8, v10
	v_sin_f32_e32 v10, v10
	v_mov_b64_e32 v[28:29], v[12:13]
	v_pk_mul_f32 v[14:15], v[10:11], v[30:31]
	s_nop 0
	v_pk_fma_f32 v[14:15], v[8:9], v[42:43], v[14:15] neg_lo:[0,0,1] neg_hi:[0,0,1]
	v_pk_mul_f32 v[8:9], v[8:9], v[30:31]
	s_nop 0
	v_pk_fma_f32 v[30:31], v[10:11], v[42:43], v[8:9]
	v_mul_f32_e32 v8, v152, v7
	v_floor_f32_e32 v8, v8
	v_fma_f32 v8, v152, v7, -v8
	v_cos_f32_e32 v9, v8
	v_sin_f32_e32 v11, v8
	v_mul_f32_e32 v8, v154, v7
	v_floor_f32_e32 v8, v8
	v_fma_f32 v10, v154, v7, -v8
	v_cos_f32_e32 v8, v10
	v_sin_f32_e32 v10, v10
	v_mov_b64_e32 v[42:43], v[14:15]
	v_pk_mul_f32 v[16:17], v[10:11], v[34:35]
	s_nop 0
	v_pk_fma_f32 v[16:17], v[8:9], v[40:41], v[16:17] neg_lo:[0,0,1] neg_hi:[0,0,1]
	v_pk_mul_f32 v[8:9], v[8:9], v[34:35]
	s_nop 0
	v_pk_fma_f32 v[34:35], v[10:11], v[40:41], v[8:9]
	v_mul_f32_e32 v8, v156, v7
	v_floor_f32_e32 v8, v8
	v_fma_f32 v8, v156, v7, -v8
	v_cos_f32_e32 v9, v8
	v_sin_f32_e32 v11, v8
	v_mul_f32_e32 v8, v158, v7
	v_floor_f32_e32 v8, v8
	v_fma_f32 v7, v158, v7, -v8
	v_sin_f32_e32 v10, v7
	v_cos_f32_e32 v8, v7
	v_mov_b64_e32 v[40:41], v[16:17]
	v_pk_mul_f32 v[18:19], v[10:11], v[36:37]
	s_nop 0
	v_pk_fma_f32 v[18:19], v[8:9], v[38:39], v[18:19] neg_lo:[0,0,1] neg_hi:[0,0,1]
	v_pk_mul_f32 v[8:9], v[8:9], v[36:37]
	s_nop 0
	v_pk_fma_f32 v[36:37], v[10:11], v[38:39], v[8:9]
	v_mov_b64_e32 v[38:39], v[18:19]
; __device__ __forceinline__ float lo16(unsigned u) { return __uint_as_float(u << 16); }
; __device__ __forceinline__ float hi16(unsigned u) { return __uint_as_float(u & 0xffff0000u); }
; __device__ void phase_swa_mfma(const Params& p, int l, char* smem, int vb, int nvb, int pend, int oz) {
;     ...
;         for (int qt2 = 0; qt2 < 2; ++qt2) {
;             const int tq = qt * 64 + 32 * qsub + 16 * qt2 + li;
;             const bf16_t* qp = U + (qbase + tq) * LDU + C_SQ + hq * 64 + 8 * g;
;             const u32x4 r0 = *(const u32x4*)qp, r1 = *(const u32x4*)(qp + 32);
;             float x1[8], x2[8];
; #pragma unroll
;             for (int w = 0; w < 4; ++w) {
;                 x1[2 * w] = lo16(r0[w]); x1[2 * w + 1] = hi16(r0[w]);
;                 x2[2 * w] = lo16(r1[w]); x2[2 * w + 1] = hi16(r1[w]);
;             }
;             if (!cq) {
;                 const float pos = (g < 2) ? (float)(tq >> 6) : (float)(tq & 63);
; #pragma unroll
;                 for (int j = 0; j < 8; ++j) {
;                     float rev = pos * invq[j];
;                     rev -= floorf(rev);
;                     const float cs = __builtin_amdgcn_cosf(rev), sn = __builtin_amdgcn_sinf(rev);
;                     const float a1 = x1[j], a2 = x2[j];
;                     x1[j] = a1 * cs - a2 * sn;
;                     x2[j] = a1 * sn + a2 * cs;
;                 }
;             }
.LBB0_185:
	v_or_b32_e32 v126, 16, v120
	v_mov_b32_e32 v127, v3
	v_lshl_add_u64 v[8:9], s[20:21], 0, v[126:127]
	v_mov_b64_e32 v[10:11], s[34:35]
	v_mad_u64_u32 v[108:109], s[20:21], v8, s92, v[10:11]
	v_mov_b32_e32 v8, v109
	s_lshl_b32 s24, s80, 6
	v_mad_u64_u32 v[8:9], s[20:21], v9, s92, v[8:9]
	v_mov_b32_e32 v109, v8
	s_lshl_b32 s20, s24, 1
	s_mov_b32 s21, s97
	v_lshl_add_u64 v[8:9], v[108:109], 0, s[20:21]
	v_mov_b32_e32 v7, v3
	v_lshl_add_u64 v[10:11], v[8:9], 0, v[6:7]
	v_add_co_u32_e32 v6, vcc, s22, v10
	s_mov_b32 s81, 0
	s_nop 0
	v_addc_co_u32_e32 v7, vcc, 0, v11, vcc
	v_lshl_add_u64 v[10:11], v[10:11], 0, s[4:5]
	s_and_b64 vcc, exec, s[42:43]
	s_waitcnt vmcnt(0)
	v_mov_b64_e32 v[6:7], v[226:227]
	v_mov_b64_e32 v[8:9], v[228:229]
	v_mov_b64_e32 v[10:11], v[230:231]
	v_mov_b64_e32 v[12:13], v[232:233]
	v_and_b32_e32 v20, 0xffff0000, v6
	v_lshlrev_b32_e32 v21, 16, v6
	v_and_b32_e32 v24, 0xffff0000, v10
	v_lshlrev_b32_e32 v25, 16, v10
	v_and_b32_e32 v50, 0xffff0000, v7
	v_lshlrev_b32_e32 v51, 16, v7
	v_and_b32_e32 v22, 0xffff0000, v11
	v_lshlrev_b32_e32 v23, 16, v11
	v_and_b32_e32 v48, 0xffff0000, v8
	v_lshlrev_b32_e32 v49, 16, v8
	v_and_b32_e32 v26, 0xffff0000, v12
	v_lshlrev_b32_e32 v27, 16, v12
	v_and_b32_e32 v46, 0xffff0000, v9
	v_lshlrev_b32_e32 v47, 16, v9
	v_and_b32_e32 v44, 0xffff0000, v13
	v_lshlrev_b32_e32 v45, 16, v13
	s_cbranch_vccnz .LBB0_187
	v_and_b32_e32 v6, 63, v126
	v_mov_b32_e32 v7, s57
	v_cndmask_b32_e64 v6, v6, v7, s[36:37]
	v_cvt_f32_u32_e32 v16, v6
	s_mov_b32 s81, 5
	s_mov_b64 s[50:51], s[46:47]
	v_mul_f32_e32 v6, v1, v16
	v_floor_f32_e32 v6, v6
	v_fma_f32 v6, v1, v16, -v6
	v_cos_f32_e32 v7, v6
	v_sin_f32_e32 v9, v6
	v_mul_f32_e32 v6, v103, v16
	v_floor_f32_e32 v6, v6
	v_fma_f32 v8, v103, v16, -v6
	v_cos_f32_e32 v6, v8
	v_sin_f32_e32 v8, v8
	s_nop 0
	v_pk_mul_f32 v[10:11], v[8:9], v[24:25]
	s_nop 0
	v_pk_fma_f32 v[10:11], v[6:7], v[20:21], v[10:11] neg_lo:[0,0,1] neg_hi:[0,0,1]
	v_pk_mul_f32 v[6:7], v[6:7], v[24:25]
	s_nop 0
	v_pk_fma_f32 v[24:25], v[8:9], v[20:21], v[6:7]
	v_mul_f32_e32 v6, v148, v16
	v_floor_f32_e32 v6, v6
	v_fma_f32 v6, v148, v16, -v6
	v_cos_f32_e32 v7, v6
	v_sin_f32_e32 v9, v6
	v_mul_f32_e32 v6, v150, v16
	v_floor_f32_e32 v6, v6
	v_fma_f32 v8, v150, v16, -v6
	v_cos_f32_e32 v6, v8
	v_sin_f32_e32 v8, v8
	v_mov_b64_e32 v[20:21], v[10:11]
	v_pk_mul_f32 v[12:13], v[8:9], v[22:23]
	s_nop 0
	v_pk_fma_f32 v[12:13], v[6:7], v[50:51], v[12:13] neg_lo:[0,0,1] neg_hi:[0,0,1]
	v_pk_mul_f32 v[6:7], v[6:7], v[22:23]
	s_nop 0
	v_pk_fma_f32 v[22:23], v[8:9], v[50:51], v[6:7]
	v_mul_f32_e32 v6, v152, v16
	v_floor_f32_e32 v6, v6
	v_fma_f32 v6, v152, v16, -v6
	v_cos_f32_e32 v7, v6
	v_sin_f32_e32 v9, v6
	v_mul_f32_e32 v6, v154, v16
	v_floor_f32_e32 v6, v6
	v_fma_f32 v8, v154, v16, -v6
	v_cos_f32_e32 v6, v8
	v_sin_f32_e32 v8, v8
	v_mov_b64_e32 v[50:51], v[12:13]
	v_pk_mul_f32 v[14:15], v[8:9], v[26:27]
	s_nop 0
	v_pk_fma_f32 v[14:15], v[6:7], v[48:49], v[14:15] neg_lo:[0,0,1] neg_hi:[0,0,1]
	v_pk_mul_f32 v[6:7], v[6:7], v[26:27]
	s_nop 0
	v_pk_fma_f32 v[26:27], v[8:9], v[48:49], v[6:7]
	v_mul_f32_e32 v6, v156, v16
	v_floor_f32_e32 v6, v6
	v_fma_f32 v6, v156, v16, -v6
	v_cos_f32_e32 v7, v6
	v_sin_f32_e32 v9, v6
	v_mul_f32_e32 v6, v158, v16
	v_floor_f32_e32 v6, v6
	v_fma_f32 v8, v158, v16, -v6
	v_cos_f32_e32 v6, v8
	v_sin_f32_e32 v8, v8
	v_mov_b64_e32 v[48:49], v[14:15]
	v_pk_mul_f32 v[16:17], v[8:9], v[44:45]
	s_nop 0
	v_pk_fma_f32 v[16:17], v[6:7], v[46:47], v[16:17] neg_lo:[0,0,1] neg_hi:[0,0,1]
	v_pk_mul_f32 v[6:7], v[6:7], v[44:45]
	s_nop 0
	v_pk_fma_f32 v[44:45], v[8:9], v[46:47], v[6:7]
	v_mov_b64_e32 v[46:47], v[16:17]
